# attention P.V: counted lgkmcnt waits so V-fragment reads of the next 32-column group stay in flight under the MFMAs; indexer threshold search: Illinois (interpolating) pivot instead of the value midpo
# speedup vs baseline: 1.0166x; 1.0064x over previous
; __device__ __forceinline__ void indexer_phase(const Frame& F, const bf16_t* QI, const bf16_t* KI, const float* WI, unsigned* MASK, const pg8::SideConv& SD) {
;     ...
;         float tau = -3.0e38f; int tiemode = 0, need = 0;
;         for (int rep20 = 0; rep20 < (REP_PHASE == 20 ? 2 : 1); ++rep20) {
;             tiemode = 0; need = 0;
;             float lo = 0.f, hiv = 0.f; int done = (tq + 1 <= TOPK) ? 1 : 0;
;             if (!done) {
;                 float mn = __builtin_inff(), mx = NEG;
; #pragma unroll
;                 for (int c = 0; c < 16; ++c) if (c < nch) {
; #pragma unroll
;                     for (int k = 0; k < 8; ++k) { const float v = sc[c * 8 + k]; mx = fmaxf(mx, v); mn = fminf(mn, (v == NEG) ? __builtin_inff() : v); } }
;                 lo = half_min(mn); mx = half_max(mx);
;                 hiv = mx + fabsf(mx) * 1e-6f + 1e-30f;
;             }
.LBB0_1667:
	s_or_b64 exec, exec, s[16:17]
	v_mov_b32_e32 v250, 0x43800000
	v_mov_b32_e32 v251, 0xc3800000
	v_mov_b32_e32 v253, 0
	s_cmpk_gt_u32 s60, 0x4ff
	s_cselect_b64 s[56:57], -1, 0
	s_cmpk_gt_u32 s60, 0x8ff
	s_cselect_b64 s[58:59], -1, 0
	s_cmpk_gt_u32 s60, 0xcff
	v_cndmask_b32_e64 v0, 0, 1, s[14:15]
	s_cselect_b64 s[60:61], -1, 0
	v_mov_b32_e32 v2, 0
	v_mov_b32_e32 v4, 0xff61b1e6
	s_mov_b32 s85, 0
	v_mov_b32_e32 v3, 0
	s_branch .LBB0_1670

; __device__ __forceinline__ void indexer_phase(const Frame& F, const bf16_t* QI, const bf16_t* KI, const float* WI, unsigned* MASK, const pg8::SideConv& SD) {
;     ...
;             for (int it = 0; it < 64 && __any(!done); ++it) {
;                 const unsigned ul = __float_as_uint(lo), uh = __float_as_uint(hiv);
;                 const unsigned kl = (ul & 0x80000000u) ? ~ul : (ul | 0x80000000u), kh = (uh & 0x80000000u) ? ~uh : (uh | 0x80000000u);
;                 const bool adj = (kh - kl) <= 1u;
;                 const unsigned km = kl + ((kh - kl) >> 1);
;                 const float kmid = __uint_as_float((km & 0x80000000u) ? (km ^ 0x80000000u) : ~km);
;                 const float fmid = 0.5f * (lo + hiv);
;                 const float mid = (it < 24 && fmid > lo && fmid < hiv) ? fmid : kmid;
;                 const float piv = adj ? hiv : mid;
;                 int lt = 0; const f32x2 pv2 = {piv, piv};
; #pragma unroll
;                 for (int gq = 0; gq < 4; ++gq) {
;                     unsigned bits = 0u;
;                     if (gq * 4 < nch) {
; #pragma unroll
;                     for (int cc = 0; cc < 4; ++cc) { const int c = gq * 4 + cc;
; #pragma unroll
;                         for (int k = 0; k < 8; k += 2) { const f32x2 d = (f32x2){sc[c * 8 + k], sc[c * 8 + k + 1]} - pv2;
;                             bits = __builtin_amdgcn_alignbit(bits, __float_as_uint(d[0]), 31); bits = __builtin_amdgcn_alignbit(bits, __float_as_uint(d[1]), 31); } }
;                     lt += 32 - __popc(bits); }
.LBB0_1670:
	v_cmp_eq_u32_e64 s[16:17], 0, v0
	s_mov_b64 vcc, s[16:17]
	s_cbranch_vccz .LBB0_1686
	v_not_b32_e32 v0, v5
	v_or_b32_e32 v1, 0x80000000, v5
	v_cmp_gt_i32_e32 vcc, 0, v5
	v_or_b32_e32 v7, 0x80000000, v6
	s_cmp_lt_u32 s85, 24
	v_cndmask_b32_e32 v0, v1, v0, vcc
	v_not_b32_e32 v1, v6
	v_cmp_gt_i32_e32 vcc, 0, v6
	s_cselect_b64 s[64:65], -1, 0
	v_mov_b32_e32 v8, 0
	v_cndmask_b32_e32 v1, v7, v1, vcc
	v_sub_u32_e32 v1, v1, v0
	v_lshrrev_b32_e32 v7, 1, v1
	v_add_u32_e32 v0, v7, v0
	v_cmp_lt_i32_e32 vcc, -1, v0
	v_cmp_lt_u32_e64 s[14:15], 1, v1
	s_nop 0
	v_cndmask_b32_e64 v7, v232, -1, vcc
	v_xor_b32_e32 v0, v7, v0
	v_sub_f32_e32 v252, v250, v251
	v_sub_f32_e32 v254, v6, v5
	v_rcp_f32_e32 v252, v252
	s_nop 1
	v_mul_f32_e32 v252, v250, v252
	v_max_f32_e32 v252, 0x3ca3d70a, v252
	v_min_f32_e32 v252, 0x3f7ae148, v252
	v_fma_f32 v7, v254, v252, v5
	v_cmp_gt_f32_e32 vcc, v7, v5
	s_and_b64 s[64:65], s[64:65], vcc
	v_cmp_lt_f32_e32 vcc, v7, v6
	s_and_b64 vcc, s[64:65], vcc
	s_nop 0
	v_cndmask_b32_e32 v7, v0, v7, vcc
	v_cmp_gt_u32_e32 vcc, 2, v1
	s_nop 1
	v_cndmask_b32_e32 v0, v7, v6, vcc
	s_andn2_b64 vcc, exec, s[54:55]
	v_mov_b32_e32 v1, v0
	s_cbranch_vccnz .LBB0_1675
	v_sub_f32_e32 v8, v212, v0
	v_sub_f32_e32 v9, v213, v1
	v_lshrrev_b32_e32 v8, 31, v8
	v_alignbit_b32 v10, v8, v9, 31
	v_sub_f32_e32 v8, v210, v0
	v_sub_f32_e32 v9, v211, v1
	v_alignbit_b32 v8, v10, v8, 31
	v_alignbit_b32 v10, v8, v9, 31
	v_sub_f32_e32 v8, v208, v0
	v_sub_f32_e32 v9, v209, v1
	v_alignbit_b32 v8, v10, v8, 31
	v_alignbit_b32 v10, v8, v9, 31
	v_sub_f32_e32 v8, v206, v0
	v_sub_f32_e32 v9, v207, v1
	v_alignbit_b32 v8, v10, v8, 31
	v_alignbit_b32 v10, v8, v9, 31
	v_sub_f32_e32 v8, v204, v0
	v_sub_f32_e32 v9, v205, v1
	v_alignbit_b32 v8, v10, v8, 31
	v_alignbit_b32 v10, v8, v9, 31
	v_sub_f32_e32 v8, v202, v0
	v_sub_f32_e32 v9, v203, v1
	v_alignbit_b32 v8, v10, v8, 31
	v_alignbit_b32 v10, v8, v9, 31
	v_sub_f32_e32 v8, v200, v0
	v_sub_f32_e32 v9, v201, v1
	v_alignbit_b32 v8, v10, v8, 31
	v_alignbit_b32 v10, v8, v9, 31
	v_sub_f32_e32 v8, v198, v0
	v_sub_f32_e32 v9, v199, v1
	v_alignbit_b32 v8, v10, v8, 31
	v_alignbit_b32 v10, v8, v9, 31
	v_sub_f32_e32 v8, v196, v0
	v_sub_f32_e32 v9, v197, v1
	v_alignbit_b32 v8, v10, v8, 31
	v_alignbit_b32 v10, v8, v9, 31
	v_sub_f32_e32 v8, v194, v0
	v_sub_f32_e32 v9, v195, v1
	v_alignbit_b32 v8, v10, v8, 31
	v_alignbit_b32 v10, v8, v9, 31
	v_sub_f32_e32 v8, v192, v0
	v_sub_f32_e32 v9, v193, v1
	v_alignbit_b32 v8, v10, v8, 31
	v_alignbit_b32 v10, v8, v9, 31
	v_sub_f32_e32 v8, v190, v0
	v_sub_f32_e32 v9, v191, v1
	v_alignbit_b32 v8, v10, v8, 31
	v_alignbit_b32 v10, v8, v9, 31
	v_sub_f32_e32 v8, v188, v0
	v_sub_f32_e32 v9, v189, v1
	v_alignbit_b32 v8, v10, v8, 31
	v_alignbit_b32 v10, v8, v9, 31
	v_sub_f32_e32 v8, v186, v0
	v_sub_f32_e32 v9, v187, v1
	v_alignbit_b32 v8, v10, v8, 31
	v_alignbit_b32 v10, v8, v9, 31
	v_sub_f32_e32 v8, v184, v0
	v_sub_f32_e32 v9, v185, v1
	v_alignbit_b32 v8, v10, v8, 31
	v_alignbit_b32 v10, v8, v9, 31
	v_sub_f32_e32 v8, v182, v0
	v_sub_f32_e32 v9, v183, v1
	v_alignbit_b32 v8, v10, v8, 31
	v_alignbit_b32 v8, v8, v9, 31
	v_not_b32_e32 v8, v8
	v_bcnt_u32_b32 v8, v8, 0
	s_andn2_b64 vcc, exec, s[56:57]
	s_cbranch_vccz .LBB0_1676

; template <int CTRL> __device__ __forceinline__ int dpp_mov(int v) { return __builtin_amdgcn_update_dpp(0, v, CTRL, 0xF, 0xF, true); }
; __device__ __forceinline__ int half_sum_rl(int v, int hi) {
;     v += dpp_mov<0xB1>(v); v += dpp_mov<0x4E>(v); v += dpp_mov<0x141>(v); v += dpp_mov<0x140>(v);
;     const int a = __builtin_amdgcn_readlane(v, 0) + __builtin_amdgcn_readlane(v, 16), b = __builtin_amdgcn_readlane(v, 32) + __builtin_amdgcn_readlane(v, 48);
;     return hi ? b : a;
; }
; __device__ __forceinline__ void indexer_phase(const Frame& F, const bf16_t* QI, const bf16_t* KI, const float* WI, unsigned* MASK, const pg8::SideConv& SD) {
;     ...
;                 const int cnt = half_sum_rl(lt, hi);
;                 if (!done) {
;                     if (adj) { tau = lo; tiemode = 1; need = TOPK - cnt; done = 1; }
;                     else if (cnt == TOPK) { tau = mid; done = 1; }
;                     else if (cnt > TOPK) lo = mid; else hiv = mid;
;                 }
.LBB0_1679:
	s_nop 1
	v_add_u32_dpp v0, v8, v8 quad_perm:[1,0,3,2] row_mask:0xf bank_mask:0xf bound_ctrl:1
	s_nop 1
	v_add_u32_dpp v0, v0, v0 quad_perm:[2,3,0,1] row_mask:0xf bank_mask:0xf bound_ctrl:1
	s_nop 1
	v_add_u32_dpp v0, v0, v0 row_half_mirror row_mask:0xf bank_mask:0xf bound_ctrl:1
	s_nop 1
	v_add_u32_dpp v0, v0, v0 row_mirror row_mask:0xf bank_mask:0xf bound_ctrl:1
	s_nop 0
	v_readlane_b32 s86, v0, 0
	v_readlane_b32 s87, v0, 16
	v_readlane_b32 s88, v0, 32
	v_readlane_b32 s89, v0, 48
	v_mov_b32_e32 v0, 1
	s_and_saveexec_b64 s[64:65], s[16:17]
	s_cbranch_execz .LBB0_1669
	s_add_i32 s16, s87, s86
	s_add_i32 s17, s89, s88
	v_mov_b32_e32 v0, s17
	v_mov_b32_e32 v1, s16
	v_cndmask_b32_e64 v1, v0, v1, s[0:1]
	s_and_saveexec_b64 s[16:17], s[14:15]
	s_xor_b64 s[14:15], exec, s[16:17]
	s_cbranch_execz .LBB0_1684
	v_cmp_ne_u32_e32 vcc, s77, v1
	v_mov_b32_e32 v0, 1
	s_and_saveexec_b64 s[16:17], vcc
	v_cmp_lt_i32_e32 vcc, s77, v1
	v_mov_b32_e32 v0, 0
	s_nop 0
	v_cndmask_b32_e32 v6, v7, v6, vcc
	v_cndmask_b32_e32 v5, v5, v7, vcc
	v_mov_b32_e32 v7, v4
	v_cvt_f32_i32_e32 v252, v1
	v_cmp_eq_u32_e64 s[98:99], 1, v253
	v_mul_f32_e32 v254, 0.5, v251
	v_add_f32_e32 v252, 0xc3800000, v252
	s_and_b64 s[98:99], s[98:99], vcc
	s_nop 1
	v_cndmask_b32_e64 v251, v251, v254, s[98:99]
	v_cmp_eq_u32_e64 s[98:99], 2, v253
	v_mul_f32_e32 v254, 0.5, v250
	s_nop 0
	s_andn2_b64 s[98:99], s[98:99], vcc
	s_nop 1
	v_cndmask_b32_e64 v250, v250, v254, s[98:99]
	v_cndmask_b32_e32 v250, v250, v252, vcc
	v_cndmask_b32_e32 v251, v252, v251, vcc
	v_cndmask_b32_e64 v253, 2, 1, vcc
	s_or_b64 exec, exec, s[16:17]

; template <int KB, int QREG>
; __device__ __forceinline__ void qkt(f32x16& p0, f32x16& p1, const char* K_lds, int r32, int hi, const bf16x8* qr, const char* qlds) {
;     p0 = f32x16{}; p1 = f32x16{};
;     const char* kb[4];
; #pragma unroll
;     for (int dd = 0; dd < 4; ++dd) kb[dd] = K_lds + KB * SHM_K + KSWZ(r32, (dd * 16 + hi * 8) * 2);
; #pragma unroll
;     for (int d0 = 0; d0 < 8; ++d0) { const char* a = kb[d0 & 3] + (d0 >> 2) * 128;
;         bf16x8 b0 = *reinterpret_cast<const bf16x8*>(a);
;         bf16x8 b1 = *reinterpret_cast<const bf16x8*>(a + 32 * 256);
;         const bf16x8 qf = (d0 < QREG) ? qr[d0 < QREG ? d0 : 0] : *reinterpret_cast<const bf16x8*>(qlds + (d0 - QREG) * 1024);
;         p0 = __builtin_amdgcn_mfma_f32_32x32x16_bf16(b0, qf, p0, 0, 0, 0);
;         p1 = __builtin_amdgcn_mfma_f32_32x32x16_bf16(b1, qf, p1, 0, 0, 0); }
; }
; template <int VB>
; __device__ __forceinline__ void pv_tile(f32x16* o, int vb0, bf16x8 pa0, bf16x8 pa1, bf16x8 pa2, bf16x8 pa3) {
;     ...
;     PV_D0(0); PV_D0(1); PV_D0(2); PV_D0(3);
.LBB0_1812:
	ds_read_b128 v[2:5], v213 offset:49152
	ds_read_b128 v[250:253], v212 offset:49152
	ds_read_b128 v[6:9], v213 offset:49280
	v_add_f32_e32 v0, 0, v126
	v_add_f32_e32 v0, v127, v0
	v_add_f32_e32 v0, v124, v0
	s_waitcnt lgkmcnt(2)
	v_mfma_f32_32x32x16_bf16 v[96:111], v[2:5], v[164:167], 0
	ds_read_b128 v[2:5], v213 offset:57344
	ds_read_b128 v[10:13], v212 offset:49280
	v_add_f32_e32 v0, v125, v0
	v_add_f32_e32 v0, v122, v0
	v_add_f32_e32 v0, v123, v0
	v_add_f32_e32 v0, v120, v0
	v_add_f32_e32 v0, v121, v0
	v_add_f32_e32 v0, v118, v0
	s_waitcnt lgkmcnt(3)
	v_mfma_f32_32x32x16_bf16 v[96:111], v[250:253], v[160:163], v[96:111]
	ds_read_b128 v[250:253], v212 offset:57344
	ds_read_b128 v[128:131], v213 offset:57472
	v_add_f32_e32 v0, v119, v0
	v_add_f32_e32 v0, v116, v0
	v_add_f32_e32 v0, v117, v0
	v_add_f32_e32 v0, v114, v0
	v_add_f32_e32 v0, v115, v0
	v_add_f32_e32 v0, v112, v0
	s_waitcnt lgkmcnt(3)
	v_mfma_f32_32x32x16_bf16 v[80:95], v[2:5], v[164:167], 0
	ds_read_b128 v[2:5], v211 offset:49152
	ds_read_b128 v[132:135], v212 offset:57472
	v_add_f32_e32 v0, v113, v0
	s_waitcnt lgkmcnt(3)
	v_mfma_f32_32x32x16_bf16 v[80:95], v[250:253], v[160:163], v[80:95]
	ds_read_b128 v[250:253], v211 offset:57344
	ds_read_b128 v[136:139], v211 offset:49280
	s_waitcnt lgkmcnt(3)
	v_mfma_f32_32x32x16_bf16 v[96:111], v[2:5], v[156:159], v[96:111]
	ds_read_b128 v[2:5], v210 offset:49152
	ds_read_b128 v[140:143], v211 offset:57472
	s_waitcnt lgkmcnt(3)
	v_mfma_f32_32x32x16_bf16 v[80:95], v[250:253], v[156:159], v[80:95]
	ds_read_b128 v[250:253], v210 offset:57344
	ds_read_b128 v[220:223], v210 offset:49280
	s_waitcnt lgkmcnt(3)
	v_mfma_f32_32x32x16_bf16 v[96:111], v[2:5], v[152:155], v[96:111]
	ds_read_b128 v[224:227], v210 offset:57472
	s_waitcnt lgkmcnt(2)
	v_mfma_f32_32x32x16_bf16 v[80:95], v[250:253], v[152:155], v[80:95]
	v_mfma_f32_32x32x16_bf16 v[96:111], v[6:9], v[148:151], v[96:111]
	ds_read_b128 v[2:5], v208
	ds_read_b128 v[6:9], v208 offset:1024
	v_cvt_pk_bf16_f32 v126, v126, v127
	v_cvt_pk_bf16_f32 v127, v124, v125
	v_exp_f32_e32 v124, v172
	v_exp_f32_e32 v125, v173
	v_mfma_f32_32x32x16_bf16 v[80:95], v[128:131], v[148:151], v[80:95]
	v_cvt_pk_bf16_f32 v128, v122, v123
	v_exp_f32_e32 v122, v174
	v_exp_f32_e32 v123, v175
	v_exp_f32_e32 v129, v170
	v_exp_f32_e32 v130, v171
	v_exp_f32_e32 v131, v168
	v_permlane32_swap_b32_e32 v126, v128
	v_mfma_f32_32x32x16_bf16 v[96:111], v[10:13], v[144:147], v[96:111]
	v_exp_f32_e32 v10, v178
	v_exp_f32_e32 v11, v179
	v_exp_f32_e32 v12, v176
	v_exp_f32_e32 v13, v177
	v_mfma_f32_32x32x16_bf16 v[80:95], v[132:135], v[144:147], v[80:95]
	v_bfe_i32 v133, v195, 16, 1
	v_exp_f32_e32 v132, v169
	s_waitcnt lgkmcnt(1)
	v_mfma_f32_32x32x16_bf16 v[96:111], v[136:139], v[2:5], v[96:111]
	v_mfma_f32_32x32x16_bf16 v[80:95], v[140:143], v[2:5], v[80:95]
	v_exp_f32_e32 v2, v182
	v_exp_f32_e32 v3, v183
	v_exp_f32_e32 v4, v180
	v_exp_f32_e32 v5, v181
	v_and_b32_e32 v2, v133, v2
	v_bfe_i32 v133, v195, 17, 1
	v_add_f32_e32 v0, v0, v2
	v_and_b32_e32 v3, v133, v3
	v_bfe_i32 v133, v195, 18, 1
	v_add_f32_e32 v0, v0, v3
	v_and_b32_e32 v4, v133, v4
	v_bfe_i32 v133, v195, 19, 1
	v_add_f32_e32 v0, v0, v4
	v_and_b32_e32 v5, v133, v5
	v_bfe_i32 v133, v195, 20, 1
	v_add_f32_e32 v0, v0, v5
	v_and_b32_e32 v10, v133, v10
	v_bfe_i32 v133, v195, 21, 1
	v_add_f32_e32 v0, v0, v10
	v_and_b32_e32 v11, v133, v11
	v_bfe_i32 v133, v195, 22, 1
	v_add_f32_e32 v0, v0, v11
	v_and_b32_e32 v12, v133, v12
	v_bfe_i32 v133, v195, 23, 1
	v_add_f32_e32 v0, v0, v12
	v_and_b32_e32 v13, v133, v13
	v_bfe_i32 v133, v195, 24, 1
	v_add_f32_e32 v0, v0, v13
	v_and_b32_e32 v122, v133, v122
	v_bfe_i32 v133, v195, 25, 1
	v_add_f32_e32 v0, v0, v122
	v_and_b32_e32 v123, v133, v123
	v_bfe_i32 v133, v195, 26, 1
	v_add_f32_e32 v0, v0, v123
	v_and_b32_e32 v124, v133, v124
	v_bfe_i32 v133, v195, 27, 1
	s_waitcnt lgkmcnt(0)
	v_mfma_f32_32x32x16_bf16 v[96:111], v[220:223], v[6:9], v[96:111]
	v_and_b32_e32 v125, v133, v125
	v_bfe_i32 v133, v195, 28, 1
	v_add_f32_e32 v0, v0, v124
	v_and_b32_e32 v133, v133, v129
	v_add_f32_e32 v0, v0, v125
	v_bfe_i32 v129, v195, 29, 1
	v_add_f32_e32 v0, v0, v133
	v_mfma_f32_32x32x16_bf16 v[80:95], v[224:227], v[6:9], v[80:95]
	v_and_b32_e32 v130, v129, v130
	v_bfe_i32 v129, v195, 30, 1
	v_add_f32_e32 v0, v0, v130
	v_and_b32_e32 v131, v129, v131
	v_bfe_i32 v129, v195, 31, 1
	v_add_f32_e32 v0, v0, v131
	v_and_b32_e32 v132, v129, v132
	v_add_f32_e32 v189, v0, v132
	v_mov_b32_e32 v219, v189
	v_cvt_pk_bf16_f32 v129, v120, v121
	v_cvt_pk_bf16_f32 v118, v118, v119
	v_cvt_pk_bf16_f32 v119, v116, v117
	v_cvt_pk_bf16_f32 v120, v114, v115
	v_cvt_pk_bf16_f32 v121, v112, v113
	v_cvt_pk_bf16_f32 v112, v2, v3
	v_cvt_pk_bf16_f32 v113, v4, v5
	v_cvt_pk_bf16_f32 v114, v10, v11
	v_cvt_pk_bf16_f32 v115, v12, v13
	v_cvt_pk_bf16_f32 v122, v122, v123
	v_cvt_pk_bf16_f32 v123, v124, v125
	v_cvt_pk_bf16_f32 v124, v133, v130
	v_cvt_pk_bf16_f32 v125, v131, v132
	s_nop 1
	v_permlane32_swap_b32_e32 v189, v219
	v_permlane32_swap_b32_e32 v127, v129
	v_permlane32_swap_b32_e32 v118, v120
	v_permlane32_swap_b32_e32 v119, v121
	v_permlane32_swap_b32_e32 v112, v114
	v_permlane32_swap_b32_e32 v113, v115
	v_permlane32_swap_b32_e32 v122, v124
	v_permlane32_swap_b32_e32 v123, v125
	v_add_u32_e32 v4, 32, v196
	v_add_u32_e32 v0, -2, v194
	v_ashrrev_i32_e32 v197, 31, v196
	v_ashrrev_i32_e32 v5, 31, v4
	v_lshl_add_u64 v[2:3], v[0:1], 2, s[44:45]
	v_lshlrev_b64 v[10:11], 10, v[196:197]
	v_lshlrev_b64 v[12:13], 10, v[4:5]
	global_load_dword v217, v[2:3], off
	v_lshl_add_u64 v[2:3], v[14:15], 0, v[10:11]
	v_lshl_add_u64 v[6:7], v[14:15], 0, v[12:13]
	v_lshl_add_u64 v[10:11], v[192:193], 0, v[10:11]
	global_load_dwordx4 v[2:5], v[2:3], off
	s_nop 0
	global_load_dwordx4 v[6:9], v[6:7], off
	v_lshl_add_u64 v[116:117], v[192:193], 0, v[12:13]
	global_load_dwordx4 v[10:13], v[10:11], off
	s_nop 0
	global_load_dwordx4 v[168:171], v[116:117], off
	ds_read_b64_tr_b16 v[130:131], v206 offset:0
	ds_read_b64_tr_b16 v[132:133], v206 offset:0x800
	ds_read_b64_tr_b16 v[134:135], v206 offset:0x1000
	ds_read_b64_tr_b16 v[136:137], v206 offset:0x1800
	ds_read_b64_tr_b16 v[138:139], v206 offset:0x2000
	ds_read_b64_tr_b16 v[140:141], v206 offset:0x2800
	ds_read_b64_tr_b16 v[172:173], v206 offset:0x3000
	ds_read_b64_tr_b16 v[174:175], v206 offset:0x3800
	s_nop 0
	s_waitcnt lgkmcnt(6)
; template <int VB>
; __device__ __forceinline__ void pv_tile(f32x16* o, int vb0, bf16x8 pa0, bf16x8 pa1, bf16x8 pa2, bf16x8 pa3) {
;     ...
;     PV_D0(0); PV_D0(1); PV_D0(2); PV_D0(3);
	v_mfma_f32_32x32x16_bf16 v[64:79], v[126:129], v[130:133], v[64:79]
	ds_read_b64_tr_b16 v[130:131], v206 offset:0x200
	ds_read_b64_tr_b16 v[132:133], v206 offset:0xa00
	s_waitcnt lgkmcnt(6)
	v_mfma_f32_32x32x16_bf16 v[64:79], v[118:121], v[134:137], v[64:79]
	ds_read_b64_tr_b16 v[134:135], v206 offset:0x1200
	ds_read_b64_tr_b16 v[136:137], v206 offset:0x1a00
	s_waitcnt lgkmcnt(6)
	v_mfma_f32_32x32x16_bf16 v[64:79], v[112:115], v[138:141], v[64:79]
	ds_read_b64_tr_b16 v[138:139], v206 offset:0x2200
	ds_read_b64_tr_b16 v[140:141], v206 offset:0x2a00
	ds_read_b64_tr_b16 v[176:177], v206 offset:0x3200
	ds_read_b64_tr_b16 v[178:179], v206 offset:0x3a00
	s_waitcnt lgkmcnt(8)
	v_mfma_f32_32x32x16_bf16 v[64:79], v[122:125], v[172:175], v[64:79]
	s_waitcnt lgkmcnt(6)
	v_mfma_f32_32x32x16_bf16 v[48:63], v[126:129], v[130:133], v[48:63]
	ds_read_b64_tr_b16 v[130:131], v206 offset:0x400
	ds_read_b64_tr_b16 v[132:133], v206 offset:0xc00
	s_waitcnt lgkmcnt(6)
	v_mfma_f32_32x32x16_bf16 v[48:63], v[118:121], v[134:137], v[48:63]
	ds_read_b64_tr_b16 v[134:135], v206 offset:0x1400
	ds_read_b64_tr_b16 v[136:137], v206 offset:0x1c00
	s_waitcnt lgkmcnt(6)
	v_mfma_f32_32x32x16_bf16 v[48:63], v[112:115], v[138:141], v[48:63]
	ds_read_b64_tr_b16 v[138:139], v206 offset:0x2400
	ds_read_b64_tr_b16 v[140:141], v206 offset:0x2c00
	ds_read_b64_tr_b16 v[172:173], v206 offset:0x3400
	ds_read_b64_tr_b16 v[174:175], v206 offset:0x3c00
	s_waitcnt lgkmcnt(8)
	v_mfma_f32_32x32x16_bf16 v[48:63], v[122:125], v[176:179], v[48:63]
	s_waitcnt lgkmcnt(6)
	v_mfma_f32_32x32x16_bf16 v[32:47], v[126:129], v[130:133], v[32:47]
	ds_read_b64_tr_b16 v[130:131], v206 offset:0x600
	ds_read_b64_tr_b16 v[132:133], v206 offset:0xe00
	s_waitcnt lgkmcnt(6)
	v_mfma_f32_32x32x16_bf16 v[32:47], v[118:121], v[134:137], v[32:47]
	ds_read_b64_tr_b16 v[134:135], v206 offset:0x1600
	ds_read_b64_tr_b16 v[136:137], v206 offset:0x1e00
	s_waitcnt lgkmcnt(6)
	v_mfma_f32_32x32x16_bf16 v[32:47], v[112:115], v[138:141], v[32:47]
	ds_read_b64_tr_b16 v[138:139], v206 offset:0x2600
	ds_read_b64_tr_b16 v[140:141], v206 offset:0x2e00
	ds_read_b64_tr_b16 v[176:177], v206 offset:0x3600
	ds_read_b64_tr_b16 v[178:179], v206 offset:0x3e00
	s_waitcnt lgkmcnt(8)
	v_mfma_f32_32x32x16_bf16 v[32:47], v[122:125], v[172:175], v[32:47]
	s_waitcnt lgkmcnt(6)
	v_mfma_f32_32x32x16_bf16 v[16:31], v[126:129], v[130:133], v[16:31]
	v_max_f32_e32 v0, v97, v97
	s_waitcnt lgkmcnt(0)
	s_barrier
	s_waitcnt vmcnt(0)
	s_waitcnt vmcnt(4)
	v_bfe_i32 v116, v217, 8, 1
	v_bfe_i32 v117, v217, 10, 1
	v_mfma_f32_32x32x16_bf16 v[16:31], v[118:121], v[134:137], v[16:31]
	v_bfe_i32 v120, v217, 1, 1
	v_bfe_i32 v121, v217, 3, 1
	v_bfe_i32 v118, v217, 12, 1
	v_bfe_i32 v126, v217, 13, 1
	v_bfe_i32 v119, v217, 14, 1
	v_bfe_i32 v127, v217, 15, 1
	s_waitcnt vmcnt(3)
	ds_write_b128 v216, v[2:5]
	s_waitcnt vmcnt(2)
	ds_write_b128 v218, v[6:9]
	s_waitcnt vmcnt(1)
	ds_write_b128 v204, v[10:13] offset:32768
	s_waitcnt vmcnt(0)
	ds_write_b128 v204, v[168:171] offset:40960
	v_mfma_f32_32x32x16_bf16 v[16:31], v[112:115], v[138:141], v[16:31]
	v_max_f32_e32 v112, v96, v96
	v_max_f32_e32 v0, v112, v0
	v_max3_f32 v0, v0, v98, v99
	v_max3_f32 v0, v0, v100, v101
	v_max3_f32 v0, v0, v102, v103
	v_max3_f32 v0, v0, v104, v105
	v_max3_f32 v0, v0, v106, v107
	v_max3_f32 v0, v0, v108, v109
	v_max3_f32 v0, v0, v110, v111
	v_max3_f32 v0, v0, v80, v81
	v_max3_f32 v0, v0, v82, v83
	v_max3_f32 v0, v0, v84, v85
	v_max3_f32 v0, v0, v86, v87
	v_max3_f32 v0, v0, v88, v89
	v_max3_f32 v0, v0, v90, v91
	v_max3_f32 v0, v0, v92, v93
	v_max3_f32 v0, v0, v94, v95
	v_mov_b32_e32 v112, v0
	s_nop 1
	v_permlane32_swap_b32_e32 v0, v112
	v_max_f32_e32 v112, v112, v112
	v_max_f32_e32 v0, v0, v0
	v_max_f32_e32 v0, v0, v112
	v_sub_f32_e32 v112, v0, v184
	v_mul_f32_e32 v112, 0x3db504f3, v112
	v_cmp_ge_f32_e32 vcc, s5, v112
	v_max_f32_e32 v112, v184, v184
	v_max_f32_e32 v128, v112, v0
	v_mfma_f32_32x32x16_bf16 v[16:31], v[122:125], v[176:179], v[16:31]
	v_sub_f32_e32 v0, v184, v128
	v_mul_f32_e32 v0, 0x3e0293ee, v0
	v_exp_f32_e32 v0, v0
	s_cmp_eq_u64 vcc, exec
	s_cselect_b64 s[2:3], -1, 0
	v_bfe_i32 v112, v217, 0, 1
	v_cndmask_b32_e64 v0, v0, 1.0, s[2:3]
	v_cmp_gt_f32_e32 vcc, 1.0, v0
	v_bfe_i32 v113, v217, 2, 1
	v_bfe_i32 v114, v217, 4, 1
	v_bfe_i32 v122, v217, 5, 1
	v_bfe_i32 v115, v217, 6, 1
	v_bfe_i32 v123, v217, 7, 1
	v_bfe_i32 v124, v217, 9, 1
	v_bfe_i32 v125, v217, 11, 1
	s_cbranch_vccz .LBB0_1816
	s_and_saveexec_b64 s[48:49], s[0:1]
	ds_write_b32 v205, v0 offset:128
	s_or_b64 exec, exec, s[48:49]
	s_waitcnt lgkmcnt(0)
	v_add_u32_e32 v129, s66, v203
	ds_read_b128 v[130:133], v129 offset:224
	ds_read_b128 v[134:137], v129 offset:192
	ds_read_b128 v[138:141], v129 offset:160
	ds_read_b128 v[172:175], v129 offset:128
	s_waitcnt lgkmcnt(3)
	v_pk_mul_f32 v[76:77], v[76:77], v[130:131]
	s_waitcnt lgkmcnt(2)
	v_pk_mul_f32 v[72:73], v[72:73], v[134:135]
	s_waitcnt lgkmcnt(1)
	v_pk_mul_f32 v[68:69], v[68:69], v[138:139]
	v_pk_mul_f32 v[78:79], v[78:79], v[132:133]
	v_pk_mul_f32 v[74:75], v[74:75], v[136:137]
	v_pk_mul_f32 v[70:71], v[70:71], v[140:141]
	s_waitcnt lgkmcnt(0)
	v_pk_mul_f32 v[66:67], v[66:67], v[174:175]
	v_pk_mul_f32 v[64:65], v[64:65], v[172:173]
	v_pk_mul_f32 v[60:61], v[60:61], v[130:131]
	v_pk_mul_f32 v[56:57], v[56:57], v[134:135]
	v_pk_mul_f32 v[52:53], v[52:53], v[138:139]
	v_pk_mul_f32 v[62:63], v[62:63], v[132:133]
	v_pk_mul_f32 v[58:59], v[58:59], v[136:137]
	v_pk_mul_f32 v[54:55], v[54:55], v[140:141]
	v_pk_mul_f32 v[50:51], v[50:51], v[174:175]
	v_pk_mul_f32 v[48:49], v[48:49], v[172:173]
	v_pk_mul_f32 v[44:45], v[44:45], v[130:131]
	v_pk_mul_f32 v[40:41], v[40:41], v[134:135]
	v_pk_mul_f32 v[36:37], v[36:37], v[138:139]
	v_pk_mul_f32 v[46:47], v[46:47], v[132:133]
	v_pk_mul_f32 v[42:43], v[42:43], v[136:137]
	v_pk_mul_f32 v[38:39], v[38:39], v[140:141]
	v_pk_mul_f32 v[34:35], v[34:35], v[174:175]
	v_pk_mul_f32 v[32:33], v[32:33], v[172:173]
	v_pk_mul_f32 v[28:29], v[28:29], v[130:131]
	v_pk_mul_f32 v[24:25], v[24:25], v[134:135]
	v_pk_mul_f32 v[20:21], v[20:21], v[138:139]
	v_pk_mul_f32 v[30:31], v[30:31], v[132:133]
	v_pk_mul_f32 v[26:27], v[26:27], v[136:137]
	v_pk_mul_f32 v[22:23], v[22:23], v[140:141]
	v_pk_mul_f32 v[18:19], v[18:19], v[174:175]
	v_pk_mul_f32 v[16:17], v[16:17], v[172:173]

; template <int VB>
; __device__ __forceinline__ void pv_tile(f32x16* o, int vb0, bf16x8 pa0, bf16x8 pa1, bf16x8 pa2, bf16x8 pa3) {
;     ...
;     PV_D0(0); PV_D0(1); PV_D0(2); PV_D0(3);
.LBB0_1818:
	ds_read_b64_tr_b16 v[222:223], v206 offset:0x4000
	ds_read_b64_tr_b16 v[224:225], v206 offset:0x4800
	ds_read_b64_tr_b16 v[226:227], v206 offset:0x5000
	ds_read_b64_tr_b16 v[228:229], v206 offset:0x5800
	ds_read_b64_tr_b16 v[230:231], v206 offset:0x6000
	ds_read_b64_tr_b16 v[232:233], v206 offset:0x6800
	ds_read_b64_tr_b16 v[234:235], v206 offset:0x7000
	ds_read_b64_tr_b16 v[236:237], v206 offset:0x7800
	s_nop 0
	s_waitcnt lgkmcnt(6)
	v_mfma_f32_32x32x16_bf16 v[64:79], v[172:175], v[222:225], v[64:79]
	ds_read_b64_tr_b16 v[222:223], v206 offset:0x4200
	ds_read_b64_tr_b16 v[224:225], v206 offset:0x4a00
	s_waitcnt lgkmcnt(6)
	v_mfma_f32_32x32x16_bf16 v[64:79], v[176:179], v[226:229], v[64:79]
	ds_read_b64_tr_b16 v[226:227], v206 offset:0x5200
	ds_read_b64_tr_b16 v[228:229], v206 offset:0x5a00
	s_waitcnt lgkmcnt(6)
	v_mfma_f32_32x32x16_bf16 v[64:79], v[180:183], v[230:233], v[64:79]
	ds_read_b64_tr_b16 v[230:231], v206 offset:0x6200
	ds_read_b64_tr_b16 v[232:233], v206 offset:0x6a00
	ds_read_b64_tr_b16 v[238:239], v206 offset:0x7200
	ds_read_b64_tr_b16 v[240:241], v206 offset:0x7a00
	s_waitcnt lgkmcnt(8)
	v_mfma_f32_32x32x16_bf16 v[64:79], v[184:187], v[234:237], v[64:79]
	s_waitcnt lgkmcnt(6)
	v_mfma_f32_32x32x16_bf16 v[48:63], v[172:175], v[222:225], v[48:63]
	ds_read_b64_tr_b16 v[222:223], v206 offset:0x4400
	ds_read_b64_tr_b16 v[224:225], v206 offset:0x4c00
	s_waitcnt lgkmcnt(6)
	v_mfma_f32_32x32x16_bf16 v[48:63], v[176:179], v[226:229], v[48:63]
	ds_read_b64_tr_b16 v[226:227], v206 offset:0x5400
	ds_read_b64_tr_b16 v[228:229], v206 offset:0x5c00
	s_waitcnt lgkmcnt(6)
	v_mfma_f32_32x32x16_bf16 v[48:63], v[180:183], v[230:233], v[48:63]
	ds_read_b64_tr_b16 v[230:231], v206 offset:0x6400
	ds_read_b64_tr_b16 v[232:233], v206 offset:0x6c00
	ds_read_b64_tr_b16 v[234:235], v206 offset:0x7400
	ds_read_b64_tr_b16 v[236:237], v206 offset:0x7c00
	s_waitcnt lgkmcnt(8)
	v_mfma_f32_32x32x16_bf16 v[48:63], v[184:187], v[238:241], v[48:63]
	s_waitcnt lgkmcnt(6)
	v_mfma_f32_32x32x16_bf16 v[32:47], v[172:175], v[222:225], v[32:47]
	ds_read_b64_tr_b16 v[222:223], v206 offset:0x4600
	ds_read_b64_tr_b16 v[224:225], v206 offset:0x4e00
	s_waitcnt lgkmcnt(6)
	v_mfma_f32_32x32x16_bf16 v[32:47], v[176:179], v[226:229], v[32:47]
	ds_read_b64_tr_b16 v[226:227], v206 offset:0x5600
	ds_read_b64_tr_b16 v[228:229], v206 offset:0x5e00
	s_waitcnt lgkmcnt(6)
	v_mfma_f32_32x32x16_bf16 v[32:47], v[180:183], v[230:233], v[32:47]
	ds_read_b64_tr_b16 v[230:231], v206 offset:0x6600
	ds_read_b64_tr_b16 v[232:233], v206 offset:0x6e00
	ds_read_b64_tr_b16 v[238:239], v206 offset:0x7600
	ds_read_b64_tr_b16 v[240:241], v206 offset:0x7e00
	s_waitcnt lgkmcnt(8)
	v_mfma_f32_32x32x16_bf16 v[32:47], v[184:187], v[234:237], v[32:47]
	s_waitcnt lgkmcnt(6)
	v_mfma_f32_32x32x16_bf16 v[16:31], v[172:175], v[222:225], v[16:31]
	v_max_f32_e32 v172, v129, v129
	v_max_f32_e32 v173, v128, v128
	v_max_f32_e32 v172, v173, v172
	v_max3_f32 v172, v172, v130, v131
	v_max3_f32 v172, v172, v132, v133
	v_max3_f32 v172, v172, v134, v135
	v_max3_f32 v172, v172, v136, v137
	s_waitcnt lgkmcnt(4)
	v_mfma_f32_32x32x16_bf16 v[16:31], v[176:179], v[226:229], v[16:31]
	v_max3_f32 v172, v172, v138, v139
	v_max3_f32 v172, v172, v140, v141
	v_max3_f32 v172, v172, v142, v143
	v_max3_f32 v172, v172, v112, v113
	v_max3_f32 v172, v172, v114, v115
	v_max3_f32 v172, v172, v116, v117
	v_max3_f32 v172, v172, v118, v119
	s_waitcnt lgkmcnt(2)
	v_mfma_f32_32x32x16_bf16 v[16:31], v[180:183], v[230:233], v[16:31]
	v_max3_f32 v172, v172, v120, v121
	v_max3_f32 v172, v172, v122, v123
	v_max3_f32 v172, v172, v124, v125
	v_max3_f32 v172, v172, v126, v127
	v_mov_b32_e32 v173, v172
	s_nop 1
	v_permlane32_swap_b32_e32 v172, v173
	s_waitcnt lgkmcnt(0)
	v_mfma_f32_32x32x16_bf16 v[16:31], v[184:187], v[238:241], v[16:31]
	v_max_f32_e32 v173, v173, v173
	v_max_f32_e32 v172, v172, v172
	v_max_f32_e32 v172, v172, v173
	v_sub_f32_e32 v173, v172, v197
	v_mul_f32_e32 v173, 0x3db504f3, v173
	v_cmp_ge_f32_e32 vcc, s5, v173
	s_cmp_eq_u64 vcc, exec
	s_cselect_b64 s[2:3], -1, 0
	s_andn2_b64 vcc, exec, s[48:49]
	s_waitcnt vmcnt(0)
	v_bfe_i32 v185, v195, 0, 1
	v_bfe_i32 v186, v195, 1, 1
	v_bfe_i32 v187, v195, 2, 1
	v_bfe_i32 v222, v195, 3, 1
	v_bfe_i32 v223, v195, 4, 1
	v_bfe_i32 v224, v195, 5, 1
	v_bfe_i32 v225, v195, 6, 1
	v_bfe_i32 v226, v195, 7, 1
	v_bfe_i32 v227, v195, 8, 1
	v_bfe_i32 v228, v195, 9, 1
	v_bfe_i32 v229, v195, 10, 1
	v_bfe_i32 v230, v195, 11, 1
	v_bfe_i32 v231, v195, 12, 1
	v_bfe_i32 v232, v195, 13, 1
	v_bfe_i32 v233, v195, 14, 1
	v_bfe_i32 v234, v195, 15, 1
	s_barrier
	s_cbranch_vccnz .LBB0_1820
	s_waitcnt vmcnt(0)
	ds_write_b128 v216, v[2:5] offset:16384
	ds_write_b128 v218, v[6:9] offset:16384
	ds_write_b128 v204, v[10:13] offset:49152
	ds_write_b128 v204, v[168:171] offset:57344

; #define LAS __attribute__((address_space(3)))
; __global__ void __launch_bounds__(512, 2) fwd_kernel(Args args) {
;     extern __shared__ __attribute__((aligned(16))) unsigned char lds_raw[];
;     Frame F; F.a = &args; F.ws = args.ws; F.lds = (LAS unsigned char*)lds_raw;
;     F.wave = __builtin_amdgcn_readfirstlane(threadIdx.x >> 6); F.G = gridDim.x; F.bid = blockIdx.x;
	.amdhsa_kernel _Z10fwd_kernel4Args
		.amdhsa_group_segment_fixed_size 0
		.amdhsa_private_segment_fixed_size 0
		.amdhsa_kernarg_size 448
		.amdhsa_user_sgpr_count 2
		.amdhsa_user_sgpr_dispatch_ptr 0
		.amdhsa_user_sgpr_queue_ptr 0
		.amdhsa_user_sgpr_kernarg_segment_ptr 1
		.amdhsa_user_sgpr_dispatch_id 0
		.amdhsa_user_sgpr_kernarg_preload_length 0
		.amdhsa_user_sgpr_kernarg_preload_offset 0
		.amdhsa_user_sgpr_private_segment_size 0
		.amdhsa_uses_dynamic_stack 0
		.amdhsa_enable_private_segment 0
		.amdhsa_system_sgpr_workgroup_id_x 1
		.amdhsa_system_sgpr_workgroup_id_y 0
		.amdhsa_system_sgpr_workgroup_id_z 0
		.amdhsa_system_sgpr_workgroup_info 0
		.amdhsa_system_vgpr_workitem_id 0
		.amdhsa_next_free_vgpr 256
		.amdhsa_next_free_sgpr 100
		.amdhsa_accum_offset 256
		.amdhsa_reserve_vcc 1
		.amdhsa_float_round_mode_32 0
		.amdhsa_float_round_mode_16_64 0
		.amdhsa_float_denorm_mode_32 3
		.amdhsa_float_denorm_mode_16_64 3
		.amdhsa_dx10_clamp 1
		.amdhsa_ieee_mode 1
		.amdhsa_fp16_overflow 0
		.amdhsa_tg_split 0
		.amdhsa_exception_fp_ieee_invalid_op 0
		.amdhsa_exception_fp_denorm_src 0
		.amdhsa_exception_fp_ieee_div_zero 0
		.amdhsa_exception_fp_ieee_overflow 0
		.amdhsa_exception_fp_ieee_underflow 0
		.amdhsa_exception_fp_ieee_inexact 0
		.amdhsa_exception_int_div_zero 0
	.end_amdhsa_kernel

; #define LAS __attribute__((address_space(3)))
; __global__ void __launch_bounds__(512, 2) fwd_kernel(Args args) {
;     extern __shared__ __attribute__((aligned(16))) unsigned char lds_raw[];
;     Frame F; F.a = &args; F.ws = args.ws; F.lds = (LAS unsigned char*)lds_raw;
;     F.wave = __builtin_amdgcn_readfirstlane(threadIdx.x >> 6); F.G = gridDim.x; F.bid = blockIdx.x;
amdhsa.kernels:
  - .agpr_count:     0
    .args:
      - .offset:         0
        .size:           192
        .value_kind:     by_value
      - .offset:         192
        .size:           4
        .value_kind:     hidden_block_count_x
      - .offset:         196
        .size:           4
        .value_kind:     hidden_block_count_y
      - .offset:         200
        .size:           4
        .value_kind:     hidden_block_count_z
      - .offset:         204
        .size:           2
        .value_kind:     hidden_group_size_x
      - .offset:         206
        .size:           2
        .value_kind:     hidden_group_size_y
      - .offset:         208
        .size:           2
        .value_kind:     hidden_group_size_z
      - .offset:         210
        .size:           2
        .value_kind:     hidden_remainder_x
      - .offset:         212
        .size:           2
        .value_kind:     hidden_remainder_y
      - .offset:         214
        .size:           2
        .value_kind:     hidden_remainder_z
      - .offset:         232
        .size:           8
        .value_kind:     hidden_global_offset_x
      - .offset:         240
        .size:           8
        .value_kind:     hidden_global_offset_y
      - .offset:         248
        .size:           8
        .value_kind:     hidden_global_offset_z
      - .offset:         256
        .size:           2
        .value_kind:     hidden_grid_dims
      - .offset:         312
        .size:           4
        .value_kind:     hidden_dynamic_lds_size
    .group_segment_fixed_size: 0
    .kernarg_segment_align: 8
    .kernarg_segment_size: 448
    .language:       OpenCL C
    .language_version:
      - 2
      - 0
    .max_flat_workgroup_size: 512
    .name:           _Z10fwd_kernel4Args
    .private_segment_fixed_size: 0
    .sgpr_count:     106
    .sgpr_spill_count: 103
    .symbol:         _Z10fwd_kernel4Args.kd
    .uniform_work_group_size: 1
    .uses_dynamic_stack: false
    .vgpr_count:     256
    .vgpr_spill_count: 0
    .wavefront_size: 64
